# redundant attention unit-start workgroup barrier removed (the queue pop's two barriers already order the previous unit's exchange reads); stacked with the DPP reductions and the pre-barrier QK-init/ne
# speedup vs baseline: 1.0059x; 1.0059x over previous
.LBB0_266:
	s_or_b64 exec, exec, s[10:11]
	v_readlane_b32 s4, v254, 33
	s_waitcnt lgkmcnt(0)
	s_barrier
	v_mov_b32_e32 v0, s4
	ds_read_b32 v0, v0
	s_mov_b64 s[10:11], -1
	s_waitcnt lgkmcnt(0)
	v_readfirstlane_b32 s12, v0
	s_cmpk_gt_i32 s12, 0x1ff
	s_cbranch_scc1 .LBB0_261
	v_mov_b32_e32 v3, v178
	s_and_b32 s40, s12, 3
	v_lshlrev_b32_e32 v2, 2, v3
	v_bfe_u32 v4, v3, 5, 1
	v_and_b32_e32 v2, 12, v2
	v_bfe_u32 v5, v3, 2, 2
	v_bitop3_b32 v6, v2, v4, v5 bitop3:0x36
	v_lshlrev_b32_e32 v2, 2, v4
	v_lshrrev_b32_e32 v8, 3, v3
	v_bfe_u32 v9, v3, 1, 1
	v_or_b32_e32 v7, v2, v5
	v_and_or_b32 v8, v8, 2, v9
	v_lshlrev_b32_e32 v5, 2, v5
	v_bitop3_b32 v4, v5, v8, v4 bitop3:0x36
	v_lshlrev_b32_e32 v5, 3, v3
	v_lshlrev_b32_e32 v7, 8, v7
	v_lshlrev_b32_e32 v4, 4, v4
	v_and_b32_e32 v8, 8, v5
	v_or3_b32 v4, v7, v8, v4
	v_add_u32_e32 v4, 0x8000, v4
	v_mov_b32_e32 v9, 0x800
	v_xor_b32_e32 v7, 0x60, v4
	v_and_b32_e32 v0, 31, v3
	v_xad_u32 v16, v4, 32, v9
	v_mov_b32_e32 v17, v4
	v_xor_b32_e32 v18, 64, v4
	v_add_u32_e32 v19, 0x800, v7
	v_xor_b32_e32 v20, 0x80, v4
	v_xor_b32_e32 v7, 0xa0, v4
	v_xor_b32_e32 v22, 0xc0, v4
	v_xor_b32_e32 v4, 0xe0, v4
	v_add_u32_e32 v23, 0x800, v4
	v_lshlrev_b32_e32 v4, 8, v0
	v_add_u32_e32 v21, 0x800, v7
	v_lshl_or_b32 v241, v6, 4, v4
	v_ashrrev_i32_e32 v4, 4, v3
	s_movk_i32 s4, 0x2400
	v_and_b32_e32 v7, 15, v3
	v_mul_lo_u32 v6, v4, s4
	s_lshl_b32 s30, s40, 8
	v_lshlrev_b32_e32 v8, 3, v7
	v_and_b32_e32 v240, 63, v3
	v_or3_b32 v6, v6, v8, s30
	v_ashrrev_i32_e32 v3, 5, v3
	s_bfe_u32 s18, s12, 0x20002
	s_ashr_i32 s12, s12, 4
	v_lshl_add_u32 v214, v6, 1, v9
	v_mul_lo_u32 v6, v3, s4
	v_and_b32_e32 v5, 0xf8, v5
	s_sub_i32 s21, 31, s12
	v_or3_b32 v5, v6, v5, s30
	v_mov_b32_e32 v6, 0x1000
	v_lshl_add_u32 v216, v5, 1, v6
	v_lshlrev_b32_e32 v6, 2, v4
	s_lshl_b32 s41, s18, 12
	s_lshl_b32 s10, s21, 7
	v_and_b32_e32 v6, 12, v6
	v_bfe_u32 v8, v4, 2, 2
	s_add_i32 s10, s10, s41
	v_readlane_b32 s4, v254, 25
	v_lshlrev_b32_e32 v5, 8, v4
	v_bitop3_b32 v6, v6, v7, v8 bitop3:0x36
	s_or_b32 s20, s10, s4
	v_lshl_or_b32 v24, v6, 4, v5
	v_lshlrev_b32_e32 v4, 14, v4
	v_lshlrev_b32_e32 v5, 2, v3
	s_mul_i32 s11, s20, 0x4800
	v_and_b32_e32 v4, 0x4000, v4
	v_and_b32_e32 v5, 12, v5
	v_bfe_u32 v6, v3, 2, 2
	s_mul_hi_u32 s10, s20, 0x4800
	s_add_u32 s11, s8, s11
	v_bitop3_b32 v5, v5, v7, v6 bitop3:0x36
	v_lshl_add_u32 v3, v3, 8, v4
	s_addc_u32 s10, s9, s10
	s_lshl_b32 s42, s40, 9
	v_lshl_or_b32 v3, v5, 4, v3
	s_add_u32 s11, s11, s42
	v_add_u32_e32 v25, 0x8000, v3
	v_mov_b32_e32 v34, v240
	s_addc_u32 s42, s10, 0
	v_readlane_b32 s4, v254, 17
	v_mov_b32_e32 v212, v178
	s_mul_i32 s100, s18, 0x4800000
	s_add_u32 s100, s8, s100
	s_addc_u32 s101, s9, 0
	v_add_u32_e32 v184, 0x90000, v214
	v_add_u32_e32 v188, 0x90000, v214
	v_add_u32_e32 v192, 0x48000, v216
	v_add_u32_e32 v200, 0x90000, v216
	v_add_u32_e32 v204, 0xd8000, v216
	global_load_dwordx4 v[176:179], v214, s[100:101]
	global_load_dwordx4 v[180:183], v214, s[100:101] offset:256
	global_load_dwordx4 v[184:187], v184, s[100:101]
	global_load_dwordx4 v[188:191], v188, s[100:101] offset:256
	global_load_dwordx4 v[192:195], v192, s[100:101]
	global_load_dwordx4 v[200:203], v200, s[100:101]
	global_load_dwordx4 v[196:199], v216, s[100:101]
	global_load_dwordx4 v[204:207], v204, s[100:101]
	s_add_u32 s10, s11, s4
	v_and_b32_e32 v3, 15, v34
	v_ashrrev_i32_e32 v32, 4, v34
	s_movk_i32 s4, 0x4800
	v_lshlrev_b32_e32 v35, 4, v3
	v_mul_lo_u32 v4, v32, s4
	s_addc_u32 s11, s42, 0
	v_or_b32_e32 v4, v4, v35
	v_add_u32_e32 v48, 0x12000, v4
	v_add_u32_e32 v52, 0x24000, v4
	v_add_u32_e32 v56, 0x36000, v4
	v_add_u32_e32 v60, 0x48000, v4
	v_add_u32_e32 v64, 0x5a000, v4
	v_add_u32_e32 v68, 0x6c000, v4
	v_add_u32_e32 v72, 0x7e000, v4
	global_load_dwordx4 v[44:47], v4, s[10:11]
	global_load_dwordx4 v[48:51], v48, s[10:11]
	global_load_dwordx4 v[52:55], v52, s[10:11]
	global_load_dwordx4 v[56:59], v56, s[10:11]
	global_load_dwordx4 v[60:63], v60, s[10:11]
	global_load_dwordx4 v[64:67], v64, s[10:11]
	global_load_dwordx4 v[68:71], v68, s[10:11]
	global_load_dwordx4 v[72:75], v72, s[10:11]
	v_add_u32_e32 v8, 64, v34
	v_ashrrev_i32_e32 v33, 4, v8
	v_mul_lo_u32 v8, v33, s4
	v_or_b32_e32 v8, v8, v35
	v_add_u32_e32 v12, 0x80, v34
	v_ashrrev_i32_e32 v36, 4, v12
	v_mul_lo_u32 v12, v36, s4
	v_or_b32_e32 v12, v12, v35
	s_mov_b32 s6, 0x3e0293ee
	v_lshlrev_b32_e32 v39, 8, v33
	s_lshl_b32 s70, s21, 1
	s_add_i32 s21, s70, 2
	s_mul_i32 s18, s18, 0x4800000
	v_mov_b32_e32 v215, v1
	v_mov_b32_e32 v217, v1
	s_mov_b32 s5, 0x48000
	v_add_u32_e32 v250, 0, v24
	v_add_u32_e32 v251, 0, v25
	v_add_u32_e32 v228, 0, v17
	v_add_u32_e32 v230, 0, v16
	v_add_u32_e32 v237, 0, v18
	v_add_u32_e32 v233, 0, v19
	v_add_u32_e32 v238, 0, v20
	v_add_u32_e32 v232, 0, v21
	v_add_u32_e32 v236, 0, v22
	v_add_u32_e32 v224, 0, v23
	v_mov_b32_e32 v226, 0x41b17218
	v_xor_b32_e32 v242, 32, v241
	v_xor_b32_e32 v243, 64, v241
	v_xor_b32_e32 v244, 0x60, v241
	v_xor_b32_e32 v245, 0x80, v241
	v_xor_b32_e32 v246, 0xa0, v241
	v_xor_b32_e32 v247, 0xc0, v241
	v_xor_b32_e32 v248, 0xe0, v241
	v_mov_b32_e32 v208, 0
	s_waitcnt vmcnt(7)
	v_lshlrev_b32_e32 v26, 16, v44
	v_and_b32_e32 v27, 0xffff0000, v44
	v_pk_mul_f32 v[26:27], v[26:27], s[6:7] op_sel_hi:[1,0]
	v_lshlrev_b32_e32 v30, 16, v46
	v_cvt_pk_bf16_f32 v4, v26, v27
	v_lshlrev_b32_e32 v26, 16, v45
	v_and_b32_e32 v27, 0xffff0000, v45
	v_pk_mul_f32 v[26:27], v[26:27], s[6:7] op_sel_hi:[1,0]
	v_and_b32_e32 v31, 0xffff0000, v46
	v_cvt_pk_bf16_f32 v5, v26, v27
	v_add_u32_e32 v26, 0xc0, v34
	v_pk_mul_f32 v[30:31], v[30:31], s[6:7] op_sel_hi:[1,0]
	v_ashrrev_i32_e32 v37, 4, v26
	v_cvt_pk_bf16_f32 v6, v30, v31
	v_lshlrev_b32_e32 v30, 16, v47
	v_and_b32_e32 v31, 0xffff0000, v47
	v_mul_lo_u32 v26, v37, s4
	v_pk_mul_f32 v[30:31], v[30:31], s[6:7] op_sel_hi:[1,0]
	v_or_b32_e32 v26, v26, v35
	v_cvt_pk_bf16_f32 v7, v30, v31
	v_lshlrev_b32_e32 v31, 2, v32
	v_lshlrev_b32_e32 v30, 8, v32
	v_and_b32_e32 v31, 12, v31
	v_bfe_u32 v32, v32, 2, 2
	v_bitop3_b32 v31, v31, v3, v32 bitop3:0x36
	v_lshlrev_b32_e32 v31, 4, v31
	v_add3_u32 v30, s17, v31, v30
	ds_write_b128 v30, v[4:7]
	s_waitcnt vmcnt(6)
	v_lshlrev_b32_e32 v4, 16, v48
	v_and_b32_e32 v5, 0xffff0000, v48
	v_pk_mul_f32 v[30:31], v[4:5], s[6:7] op_sel_hi:[1,0]
	v_add_u32_e32 v4, 0x100, v34
	v_ashrrev_i32_e32 v38, 4, v4
	v_mul_lo_u32 v4, v38, s4
	v_or_b32_e32 v4, v4, v35
	v_cvt_pk_bf16_f32 v8, v30, v31
	v_lshlrev_b32_e32 v30, 16, v49
	v_and_b32_e32 v31, 0xffff0000, v49
	v_pk_mul_f32 v[30:31], v[30:31], s[6:7] op_sel_hi:[1,0]
	s_nop 0
	v_cvt_pk_bf16_f32 v9, v30, v31
	v_lshlrev_b32_e32 v30, 16, v50
	v_and_b32_e32 v31, 0xffff0000, v50
	v_pk_mul_f32 v[30:31], v[30:31], s[6:7] op_sel_hi:[1,0]
	s_nop 0
	v_cvt_pk_bf16_f32 v10, v30, v31
	v_lshlrev_b32_e32 v30, 16, v51
	v_and_b32_e32 v31, 0xffff0000, v51
	v_pk_mul_f32 v[30:31], v[30:31], s[6:7] op_sel_hi:[1,0]
	s_nop 0
	v_cvt_pk_bf16_f32 v11, v30, v31
	v_lshlrev_b32_e32 v30, 2, v33
	v_and_b32_e32 v30, 12, v30
	v_bfe_u32 v31, v33, 2, 2
	v_bitop3_b32 v30, v30, v3, v31 bitop3:0x36
	v_lshlrev_b32_e32 v40, 4, v30
	v_add_u32_e32 v30, 0x140, v34
	v_ashrrev_i32_e32 v41, 4, v30
	v_mul_lo_u32 v30, v41, s4
	v_or_b32_e32 v30, v30, v35
	v_add3_u32 v39, s17, v40, v39
	ds_write_b128 v39, v[8:11]
	s_waitcnt vmcnt(5)
	v_lshlrev_b32_e32 v8, 16, v52
	v_and_b32_e32 v9, 0xffff0000, v52
	v_lshlrev_b32_e32 v10, 16, v53
	v_and_b32_e32 v11, 0xffff0000, v53
	v_pk_mul_f32 v[8:9], v[8:9], s[6:7] op_sel_hi:[1,0]
	v_pk_mul_f32 v[10:11], v[10:11], s[6:7] op_sel_hi:[1,0]
	v_cvt_pk_bf16_f32 v8, v8, v9
	v_cvt_pk_bf16_f32 v9, v10, v11
	v_lshlrev_b32_e32 v10, 16, v54
	v_and_b32_e32 v11, 0xffff0000, v54
	v_lshlrev_b32_e32 v12, 16, v55
	v_and_b32_e32 v13, 0xffff0000, v55
	v_pk_mul_f32 v[10:11], v[10:11], s[6:7] op_sel_hi:[1,0]
	v_pk_mul_f32 v[12:13], v[12:13], s[6:7] op_sel_hi:[1,0]
	v_cvt_pk_bf16_f32 v10, v10, v11
	v_cvt_pk_bf16_f32 v11, v12, v13
	v_lshlrev_b32_e32 v12, 2, v36
	v_and_b32_e32 v12, 12, v12
	v_bfe_u32 v13, v36, 2, 2
	v_bitop3_b32 v12, v12, v3, v13 bitop3:0x36
	v_lshlrev_b32_e32 v39, 8, v36
	v_lshlrev_b32_e32 v36, 4, v12
	v_add_u32_e32 v12, 0x180, v34
	v_ashrrev_i32_e32 v40, 4, v12
	v_mul_lo_u32 v12, v40, s4
	v_or_b32_e32 v12, v12, v35
	v_add3_u32 v36, s17, v36, v39
	ds_write_b128 v36, v[8:11]
	s_waitcnt vmcnt(4)
	v_lshlrev_b32_e32 v8, 16, v56
	v_and_b32_e32 v9, 0xffff0000, v56
	v_lshlrev_b32_e32 v10, 16, v57
	v_and_b32_e32 v11, 0xffff0000, v57
	v_pk_mul_f32 v[8:9], v[8:9], s[6:7] op_sel_hi:[1,0]
	v_pk_mul_f32 v[10:11], v[10:11], s[6:7] op_sel_hi:[1,0]
	v_cvt_pk_bf16_f32 v8, v8, v9
	v_cvt_pk_bf16_f32 v9, v10, v11
	v_lshlrev_b32_e32 v10, 16, v58
	v_and_b32_e32 v11, 0xffff0000, v58
	v_lshlrev_b32_e32 v26, 16, v59
	v_and_b32_e32 v27, 0xffff0000, v59
	v_pk_mul_f32 v[10:11], v[10:11], s[6:7] op_sel_hi:[1,0]
	v_pk_mul_f32 v[26:27], v[26:27], s[6:7] op_sel_hi:[1,0]
	v_cvt_pk_bf16_f32 v10, v10, v11
	v_cvt_pk_bf16_f32 v11, v26, v27
	v_lshlrev_b32_e32 v27, 2, v37
	v_and_b32_e32 v27, 12, v27
	v_bfe_u32 v28, v37, 2, 2
	v_bitop3_b32 v27, v27, v3, v28 bitop3:0x36
	v_lshlrev_b32_e32 v26, 8, v37
	v_lshlrev_b32_e32 v27, 4, v27
	v_add3_u32 v26, s17, v27, v26
	ds_write_b128 v26, v[8:11]
	s_waitcnt vmcnt(3)
	v_lshlrev_b32_e32 v8, 16, v60
	v_and_b32_e32 v9, 0xffff0000, v60
	v_pk_mul_f32 v[8:9], v[8:9], s[6:7] op_sel_hi:[1,0]
	v_bfe_u32 v10, v38, 2, 2
	v_cvt_pk_bf16_f32 v4, v8, v9
	v_lshlrev_b32_e32 v8, 16, v61
	v_and_b32_e32 v9, 0xffff0000, v61
	v_pk_mul_f32 v[8:9], v[8:9], s[6:7] op_sel_hi:[1,0]
	v_bfe_u32 v29, v41, 2, 2
	v_cvt_pk_bf16_f32 v5, v8, v9
	v_lshlrev_b32_e32 v8, 16, v62
	v_and_b32_e32 v9, 0xffff0000, v62
	v_pk_mul_f32 v[8:9], v[8:9], s[6:7] op_sel_hi:[1,0]
	s_waitcnt vmcnt(2)
	v_lshlrev_b32_e32 v26, 16, v67
	v_cvt_pk_bf16_f32 v6, v8, v9
	v_lshlrev_b32_e32 v8, 16, v63
	v_and_b32_e32 v9, 0xffff0000, v63
	v_pk_mul_f32 v[8:9], v[8:9], s[6:7] op_sel_hi:[1,0]
	v_and_b32_e32 v27, 0xffff0000, v67
	v_cvt_pk_bf16_f32 v7, v8, v9
	v_lshlrev_b32_e32 v9, 2, v38
	v_and_b32_e32 v9, 12, v9
	v_bitop3_b32 v9, v9, v3, v10 bitop3:0x36
	v_lshlrev_b32_e32 v8, 8, v38
	v_lshlrev_b32_e32 v9, 4, v9
	v_add3_u32 v8, s17, v9, v8
	ds_write_b128 v8, v[4:7]
	v_lshlrev_b32_e32 v4, 16, v64
	v_and_b32_e32 v5, 0xffff0000, v64
	v_pk_mul_f32 v[4:5], v[4:5], s[6:7] op_sel_hi:[1,0]
	v_lshlrev_b32_e32 v6, 16, v65
	v_cvt_pk_bf16_f32 v4, v4, v5
	v_add_u32_e32 v5, 0x1c0, v34
	v_ashrrev_i32_e32 v28, 4, v5
	v_mul_lo_u32 v5, v28, s4
	v_and_b32_e32 v7, 0xffff0000, v65
	v_or_b32_e32 v5, v5, v35
	v_pk_mul_f32 v[6:7], v[6:7], s[6:7] op_sel_hi:[1,0]
	v_cvt_pk_bf16_f32 v5, v6, v7
	v_lshlrev_b32_e32 v6, 16, v66
	v_and_b32_e32 v7, 0xffff0000, v66
	v_pk_mul_f32 v[6:7], v[6:7], s[6:7] op_sel_hi:[1,0]
	v_pk_mul_f32 v[26:27], v[26:27], s[6:7] op_sel_hi:[1,0]
	v_cvt_pk_bf16_f32 v6, v6, v7
	v_cvt_pk_bf16_f32 v7, v26, v27
	v_lshlrev_b32_e32 v27, 2, v41
	v_and_b32_e32 v27, 12, v27
	v_bitop3_b32 v27, v27, v3, v29 bitop3:0x36
	v_lshlrev_b32_e32 v26, 8, v41
	v_lshlrev_b32_e32 v27, 4, v27
	v_add3_u32 v26, s17, v27, v26
	ds_write_b128 v26, v[4:7]
	s_waitcnt vmcnt(1)
	v_lshlrev_b32_e32 v4, 16, v68
	v_and_b32_e32 v5, 0xffff0000, v68
	v_lshlrev_b32_e32 v6, 16, v69
	v_and_b32_e32 v7, 0xffff0000, v69
	v_pk_mul_f32 v[4:5], v[4:5], s[6:7] op_sel_hi:[1,0]
	v_pk_mul_f32 v[6:7], v[6:7], s[6:7] op_sel_hi:[1,0]
	v_cvt_pk_bf16_f32 v4, v4, v5
	v_cvt_pk_bf16_f32 v5, v6, v7
	v_lshlrev_b32_e32 v6, 16, v70
	v_and_b32_e32 v7, 0xffff0000, v70
	v_lshlrev_b32_e32 v12, 16, v71
	v_and_b32_e32 v13, 0xffff0000, v71
	v_pk_mul_f32 v[6:7], v[6:7], s[6:7] op_sel_hi:[1,0]
	v_pk_mul_f32 v[12:13], v[12:13], s[6:7] op_sel_hi:[1,0]
	v_cvt_pk_bf16_f32 v6, v6, v7
	v_cvt_pk_bf16_f32 v7, v12, v13
	v_lshlrev_b32_e32 v13, 2, v40
	v_and_b32_e32 v13, 12, v13
	v_bfe_u32 v14, v40, 2, 2
	s_not_b32 s10, s40
	v_bitop3_b32 v13, v13, v3, v14 bitop3:0x36
	s_lshl_b32 s40, s10, 1
	v_lshlrev_b32_e32 v12, 8, v40
	v_lshlrev_b32_e32 v13, 4, v13
	s_add_u32 s10, s8, s18
	v_add3_u32 v12, s17, v13, v12
	s_addc_u32 s11, s9, 0
	ds_write_b128 v12, v[4:7]
	s_mov_b32 s4, 0x90000
	s_mov_b32 s18, 0xd8000
	s_nop 0
	v_readlane_b32 s4, v254, 26
	s_nop 0
	s_lshl_b32 s10, s12, 7
	s_add_i32 s10, s4, s10
	v_add_u32_e32 v2, s10, v2
	v_mov_b32_e32 v14, v1
	v_mov_b32_e32 v15, v1
	v_sub_u32_e32 v249, v2, v0
	v_mov_b32_e32 v0, v1
	v_mov_b32_e32 v2, v1
	v_mov_b32_e32 v12, v1
	v_mov_b32_e32 v13, v1
	s_or_b32 s18, s41, 64
	s_waitcnt vmcnt(0)
	v_lshlrev_b32_e32 v4, 16, v72
	v_and_b32_e32 v5, 0xffff0000, v72
	v_lshlrev_b32_e32 v6, 16, v73
	v_and_b32_e32 v7, 0xffff0000, v73
	v_pk_mul_f32 v[4:5], v[4:5], s[6:7] op_sel_hi:[1,0]
	v_pk_mul_f32 v[6:7], v[6:7], s[6:7] op_sel_hi:[1,0]
	v_cvt_pk_bf16_f32 v4, v4, v5
	v_cvt_pk_bf16_f32 v5, v6, v7
	v_lshlrev_b32_e32 v6, 16, v74
	v_and_b32_e32 v7, 0xffff0000, v74
	v_lshlrev_b32_e32 v8, 16, v75
	v_and_b32_e32 v9, 0xffff0000, v75
	v_cvt_f32_i32_e32 v10, s40
	v_pk_mul_f32 v[6:7], v[6:7], s[6:7] op_sel_hi:[1,0]
	v_pk_mul_f32 v[8:9], v[8:9], s[6:7] op_sel_hi:[1,0]
	v_cvt_pk_bf16_f32 v6, v6, v7
	v_cvt_pk_bf16_f32 v7, v8, v9
	v_lshlrev_b32_e32 v9, 2, v28
	v_and_b32_e32 v9, 12, v9
	v_bfe_u32 v11, v28, 2, 2
	v_bitop3_b32 v3, v9, v3, v11 bitop3:0x36
	v_exp_f32_e32 v9, v10
	v_lshlrev_b32_e32 v8, 8, v28
	v_lshlrev_b32_e32 v3, 4, v3
	v_add3_u32 v3, s17, v3, v8
	ds_write_b128 v3, v[4:7]
	v_mul_f32_e32 v218, 0x3fb8aa3b, v9
	v_mov_b32_e32 v3, v1
	v_mov_b32_e32 v4, v1
	v_mov_b32_e32 v5, v1
	v_mov_b32_e32 v6, v1
	v_mov_b32_e32 v7, v1
	v_mov_b32_e32 v8, v1
	v_mov_b32_e32 v9, v1
	v_mov_b32_e32 v10, v1
	v_mov_b32_e32 v11, v1
	v_mov_b64_e32 v[30:31], v[14:15]
	v_mov_b64_e32 v[46:47], v[14:15]
	v_mov_b64_e32 v[62:63], v[14:15]
	v_mov_b64_e32 v[78:79], v[14:15]
	v_mov_b64_e32 v[94:95], v[14:15]
	v_mov_b64_e32 v[110:111], v[14:15]
	v_mov_b64_e32 v[126:127], v[14:15]
	v_mov_b64_e32 v[142:143], v[14:15]
	s_mov_b32 s40, 0
	v_mov_b32_e32 v220, v218
	v_mov_b32_e32 v221, v218
	v_mov_b32_e32 v222, v218
	v_mov_b32_e32 v223, v218
	v_mov_b64_e32 v[28:29], v[12:13]
	v_mov_b64_e32 v[26:27], v[10:11]
	v_mov_b64_e32 v[24:25], v[8:9]
	v_mov_b64_e32 v[22:23], v[6:7]
	v_mov_b64_e32 v[20:21], v[4:5]
	v_mov_b64_e32 v[18:19], v[2:3]
	v_mov_b64_e32 v[16:17], v[0:1]
	v_mov_b64_e32 v[44:45], v[12:13]
	v_mov_b64_e32 v[42:43], v[10:11]
	v_mov_b64_e32 v[40:41], v[8:9]
	v_mov_b64_e32 v[38:39], v[6:7]
	v_mov_b64_e32 v[36:37], v[4:5]
	v_mov_b64_e32 v[34:35], v[2:3]
	v_mov_b64_e32 v[32:33], v[0:1]
	v_mov_b64_e32 v[60:61], v[12:13]
	v_mov_b64_e32 v[58:59], v[10:11]
	v_mov_b64_e32 v[56:57], v[8:9]
	v_mov_b64_e32 v[54:55], v[6:7]
	v_mov_b64_e32 v[52:53], v[4:5]
	v_mov_b64_e32 v[50:51], v[2:3]
	v_mov_b64_e32 v[48:49], v[0:1]
	v_mov_b64_e32 v[76:77], v[12:13]
	v_mov_b64_e32 v[74:75], v[10:11]
	v_mov_b64_e32 v[72:73], v[8:9]
	v_mov_b64_e32 v[70:71], v[6:7]
	v_mov_b64_e32 v[68:69], v[4:5]
	v_mov_b64_e32 v[66:67], v[2:3]
	v_mov_b64_e32 v[64:65], v[0:1]
	v_mov_b64_e32 v[92:93], v[12:13]
	v_mov_b64_e32 v[90:91], v[10:11]
	v_mov_b64_e32 v[88:89], v[8:9]
	v_mov_b64_e32 v[86:87], v[6:7]
	v_mov_b64_e32 v[84:85], v[4:5]
	v_mov_b64_e32 v[82:83], v[2:3]
	v_mov_b64_e32 v[80:81], v[0:1]
	v_mov_b64_e32 v[108:109], v[12:13]
	v_mov_b64_e32 v[106:107], v[10:11]
	v_mov_b64_e32 v[104:105], v[8:9]
	v_mov_b64_e32 v[102:103], v[6:7]
	v_mov_b64_e32 v[100:101], v[4:5]
	v_mov_b64_e32 v[98:99], v[2:3]
	v_mov_b64_e32 v[96:97], v[0:1]
	v_mov_b64_e32 v[124:125], v[12:13]
	v_mov_b64_e32 v[122:123], v[10:11]
	v_mov_b64_e32 v[120:121], v[8:9]
	v_mov_b64_e32 v[118:119], v[6:7]
	v_mov_b64_e32 v[116:117], v[4:5]
	v_mov_b64_e32 v[114:115], v[2:3]
	v_mov_b64_e32 v[112:113], v[0:1]
	v_mov_b64_e32 v[140:141], v[12:13]
	v_mov_b64_e32 v[138:139], v[10:11]
	v_mov_b64_e32 v[136:137], v[8:9]
	v_mov_b64_e32 v[134:135], v[6:7]
	v_mov_b64_e32 v[132:133], v[4:5]
	v_mov_b64_e32 v[130:131], v[2:3]
	v_mov_b64_e32 v[128:129], v[0:1]
	v_mov_b32_e32 v15, 0
	s_branch .LBB0_270
